# v049 + attention row-max exchange via v_permlane16_swap/v_permlane32_swap instead of two ds_bpermute round trips
# speedup vs baseline: 1.0064x; 1.0064x over previous
.LBB0_1072:
	s_cmp_eq_u32 s66, 0
	s_cselect_b64 vcc, -1, 0
	v_cndmask_b32_e32 v11, 0, v169, vcc
	v_sub_u32_e32 v16, 0x80, v11
	v_add_u32_e32 v11, v168, v11
	v_sub_u32_e32 v11, v150, v11
	v_add_u32_e32 v17, s68, v11
	v_cmp_le_u32_e32 vcc, v17, v16
	v_add_u32_e32 v127, 1, v17
	v_add_u32_e32 v148, 2, v17
	v_cndmask_b32_e32 v98, v181, v98, vcc
	v_cmp_le_u32_e32 vcc, v127, v16
	v_add_u32_e32 v17, 3, v17
	s_lshl_b32 s27, s40, 2
	v_cndmask_b32_e32 v99, v181, v99, vcc
	v_cmp_le_u32_e32 vcc, v148, v16
	v_max3_f32 v127, v98, s90, v99
	s_add_i32 s52, s27, s44
	v_cndmask_b32_e32 v100, v181, v100, vcc
	v_cmp_le_u32_e32 vcc, v17, v16
	s_ashr_i32 s53, s52, 31
	s_mov_b32 s51, s13
	v_cndmask_b32_e32 v101, v181, v101, vcc
	v_max3_f32 v17, v127, v100, v101
	v_add_u32_e32 v127, s69, v11
	v_cmp_le_u32_e32 vcc, v127, v16
	s_lshl_b64 s[52:53], s[52:53], 15
	s_lshl_b64 s[50:51], s[50:51], 12
	v_cndmask_b32_e32 v148, v181, v86, vcc
	v_add_u32_e32 v86, 1, v127
	v_cmp_le_u32_e32 vcc, v86, v16
	v_add_u32_e32 v86, 2, v127
	s_add_u32 s27, s52, s50
	v_cndmask_b32_e32 v87, v181, v87, vcc
	v_cmp_le_u32_e32 vcc, v86, v16
	v_add_u32_e32 v86, 3, v127
	v_max3_f32 v17, v17, v148, v87
	v_cndmask_b32_e32 v88, v181, v88, vcc
	v_cmp_le_u32_e32 vcc, v86, v16
	v_add_u32_e32 v86, s72, v11
	v_add_u32_e32 v127, 1, v86
	v_cndmask_b32_e32 v89, v181, v89, vcc
	v_cmp_le_u32_e32 vcc, v86, v16
	v_max3_f32 v17, v17, v88, v89
	s_addc_u32 s44, s53, s51
	v_cndmask_b32_e32 v110, v181, v110, vcc
	v_cmp_le_u32_e32 vcc, v127, v16
	v_add_u32_e32 v127, 2, v86
	v_add_u32_e32 v86, 3, v86
	v_cndmask_b32_e32 v111, v181, v111, vcc
	v_cmp_le_u32_e32 vcc, v127, v16
	v_max3_f32 v17, v17, v110, v111
	s_lshr_b32 s50, 0x1000, s92
	v_cndmask_b32_e32 v112, v181, v112, vcc
	v_cmp_le_u32_e32 vcc, v86, v16
	v_add_u32_e32 v86, s73, v11
	v_add_u32_e32 v127, 1, v86
	v_cndmask_b32_e32 v113, v181, v113, vcc
	v_cmp_le_u32_e32 vcc, v86, v16
	v_max3_f32 v17, v17, v112, v113
	s_mul_hi_u32 s51, s41, s50
	v_cndmask_b32_e32 v94, v181, v94, vcc
	v_cmp_le_u32_e32 vcc, v127, v16
	v_add_u32_e32 v127, 2, v86
	v_add_u32_e32 v86, 3, v86
	v_cndmask_b32_e32 v95, v181, v95, vcc
	v_cmp_le_u32_e32 vcc, v127, v16
	v_max3_f32 v17, v17, v94, v95
	s_mul_i32 s41, s41, s50
	v_cndmask_b32_e32 v96, v181, v96, vcc
	v_cmp_le_u32_e32 vcc, v86, v16
	v_add_u32_e32 v86, s80, v11
	v_add_u32_e32 v127, 1, v86
	v_cndmask_b32_e32 v97, v181, v97, vcc
	v_cmp_le_u32_e32 vcc, v86, v16
	v_max3_f32 v17, v17, v96, v97
	s_add_u32 s52, s27, s41
	v_cndmask_b32_e32 v114, v181, v114, vcc
	v_cmp_le_u32_e32 vcc, v127, v16
	v_add_u32_e32 v127, 2, v86
	v_add_u32_e32 v86, 3, v86
	v_cndmask_b32_e32 v115, v181, v115, vcc
	v_cmp_le_u32_e32 vcc, v127, v16
	v_max3_f32 v17, v17, v114, v115
	s_addc_u32 s53, s44, s51
	v_cndmask_b32_e32 v116, v181, v116, vcc
	v_cmp_le_u32_e32 vcc, v86, v16
	v_add_u32_e32 v86, s81, v11
	v_add_u32_e32 v127, 1, v86
	v_cndmask_b32_e32 v117, v181, v117, vcc
	v_cmp_le_u32_e32 vcc, v86, v16
	v_max3_f32 v17, v17, v116, v117
	s_add_i32 s27, s88, s60
	v_cndmask_b32_e32 v102, v181, v102, vcc
	v_cmp_le_u32_e32 vcc, v127, v16
	v_add_u32_e32 v127, 2, v86
	v_add_u32_e32 v86, 3, v86
	v_cndmask_b32_e32 v103, v181, v103, vcc
	v_cmp_le_u32_e32 vcc, v127, v16
	v_max3_f32 v17, v17, v102, v103
	s_add_i32 s26, s88, s26
	v_cndmask_b32_e32 v104, v181, v104, vcc
	v_cmp_le_u32_e32 vcc, v86, v16
	v_add_u32_e32 v86, s84, v11
	v_add_u32_e32 v127, 1, v86
	v_cndmask_b32_e32 v105, v181, v105, vcc
	v_cmp_le_u32_e32 vcc, v86, v16
	v_max3_f32 v17, v17, v104, v105
	s_nop 0
	v_cndmask_b32_e32 v122, v181, v122, vcc
	v_cmp_le_u32_e32 vcc, v127, v16
	v_add_u32_e32 v127, 2, v86
	v_add_u32_e32 v86, 3, v86
	v_cndmask_b32_e32 v123, v181, v123, vcc
	v_cmp_le_u32_e32 vcc, v127, v16
	v_max3_f32 v17, v17, v122, v123
	s_nop 0
	v_cndmask_b32_e32 v124, v181, v124, vcc
	v_cmp_le_u32_e32 vcc, v86, v16
	v_add_u32_e32 v86, s85, v11
	v_add_u32_e32 v127, 1, v86
	v_cndmask_b32_e32 v125, v181, v125, vcc
	v_cmp_le_u32_e32 vcc, v86, v16
	v_max3_f32 v17, v17, v124, v125
	s_nop 0
	v_cndmask_b32_e32 v118, v181, v118, vcc
	v_cmp_le_u32_e32 vcc, v127, v16
	v_add_u32_e32 v127, 2, v86
	v_add_u32_e32 v86, 3, v86
	v_cndmask_b32_e32 v119, v181, v119, vcc
	v_cmp_le_u32_e32 vcc, v127, v16
	v_max3_f32 v17, v17, v118, v119
	s_nop 0
	v_cndmask_b32_e32 v120, v181, v120, vcc
	v_cmp_le_u32_e32 vcc, v86, v16
	v_add_u32_e32 v86, s86, v11
	v_add_u32_e32 v127, 1, v86
	v_cndmask_b32_e32 v121, v181, v121, vcc
	v_cmp_le_u32_e32 vcc, v86, v16
	v_add_u32_e32 v11, s87, v11
	v_max3_f32 v17, v17, v120, v121
	v_cndmask_b32_e32 v106, v181, v106, vcc
	v_cmp_le_u32_e32 vcc, v127, v16
	v_add_u32_e32 v127, 2, v86
	v_add_u32_e32 v86, 3, v86
	v_cndmask_b32_e32 v107, v181, v107, vcc
	v_cmp_le_u32_e32 vcc, v127, v16
	v_max3_f32 v17, v17, v106, v107
	s_nop 0
	v_cndmask_b32_e32 v108, v181, v108, vcc
	v_cmp_le_u32_e32 vcc, v86, v16
	v_add_u32_e32 v86, 1, v11
	s_nop 0
	v_cndmask_b32_e32 v109, v181, v109, vcc
	v_cmp_le_u32_e32 vcc, v11, v16
	v_max3_f32 v17, v17, v108, v109
	s_nop 0
	v_cndmask_b32_e32 v90, v181, v90, vcc
	v_cmp_le_u32_e32 vcc, v86, v16
	v_add_u32_e32 v86, 2, v11
	v_add_u32_e32 v11, 3, v11
	v_cndmask_b32_e32 v127, v181, v91, vcc
	v_cmp_le_u32_e32 vcc, v86, v16
	s_nop 1
	v_cndmask_b32_e32 v149, v181, v92, vcc
	v_cmp_le_u32_e32 vcc, v11, v16
	v_max3_f32 v11, v17, v90, v127
	v_add_u32_e32 v16, s12, v168
	v_cndmask_b32_e32 v182, v181, v93, vcc
	v_max3_f32 v11, v11, v149, v182
	v_mov_b32_e32 v86, v11
	v_ashrrev_i32_e32 v17, 31, v16
	s_nop 1
	v_permlane16_swap_b32_e32 v86, v11
	v_max_f32_e32 v11, v11, v86
	v_mov_b32_e32 v86, v11
	s_nop 1
	v_permlane32_swap_b32_e32 v86, v11
	s_waitcnt lgkmcnt(0)
	v_max_f32_e32 v86, v11, v86
	v_mul_f32_e32 v183, 0xbfb8aa3b, v86
	v_fmamk_f32 v11, v98, 0x3fb8aa3b, v183
	v_exp_f32_e32 v184, v11
	v_fmamk_f32 v91, v99, 0x3fb8aa3b, v183
	v_exp_f32_e32 v185, v91
	v_fmamk_f32 v91, v100, 0x3fb8aa3b, v183
	v_exp_f32_e32 v186, v91
	v_fmamk_f32 v91, v101, 0x3fb8aa3b, v183
	v_exp_f32_e32 v187, v91
	v_fmamk_f32 v91, v148, 0x3fb8aa3b, v183
	v_add_f32_e32 v11, 0, v184
	v_exp_f32_e32 v148, v91
	v_fmamk_f32 v87, v87, 0x3fb8aa3b, v183
	v_add_f32_e32 v11, v185, v11
	v_exp_f32_e32 v188, v87
	v_fmamk_f32 v87, v88, 0x3fb8aa3b, v183
	v_add_f32_e32 v11, v186, v11
	v_exp_f32_e32 v189, v87
	v_fmamk_f32 v87, v89, 0x3fb8aa3b, v183
	v_add_f32_e32 v11, v187, v11
	v_exp_f32_e32 v190, v87
	v_fmamk_f32 v87, v110, 0x3fb8aa3b, v183
	v_add_f32_e32 v11, v148, v11
	v_exp_f32_e32 v198, v87
	v_fmamk_f32 v87, v111, 0x3fb8aa3b, v183
	v_add_f32_e32 v11, v188, v11
	v_exp_f32_e32 v199, v87
	v_fmamk_f32 v87, v112, 0x3fb8aa3b, v183
	v_add_f32_e32 v11, v189, v11
	v_exp_f32_e32 v200, v87
	v_fmamk_f32 v87, v113, 0x3fb8aa3b, v183
	v_add_f32_e32 v11, v190, v11
	v_exp_f32_e32 v201, v87
	v_fmamk_f32 v87, v94, 0x3fb8aa3b, v183
	v_add_f32_e32 v11, v198, v11
	v_exp_f32_e32 v202, v87
	v_fmamk_f32 v87, v95, 0x3fb8aa3b, v183
	v_add_f32_e32 v11, v199, v11
	v_exp_f32_e32 v203, v87
	v_fmamk_f32 v87, v96, 0x3fb8aa3b, v183
	v_add_f32_e32 v11, v200, v11
	v_exp_f32_e32 v204, v87
	v_fmamk_f32 v87, v97, 0x3fb8aa3b, v183
	v_add_f32_e32 v11, v201, v11
	v_exp_f32_e32 v205, v87
	v_fmamk_f32 v87, v114, 0x3fb8aa3b, v183
	v_add_f32_e32 v11, v202, v11
	v_exp_f32_e32 v211, v87
	v_fmamk_f32 v87, v115, 0x3fb8aa3b, v183
	v_add_f32_e32 v11, v203, v11
	v_exp_f32_e32 v216, v87
	v_fmamk_f32 v87, v116, 0x3fb8aa3b, v183
	v_add_f32_e32 v11, v204, v11
	v_exp_f32_e32 v217, v87
	v_fmamk_f32 v87, v117, 0x3fb8aa3b, v183
	v_add_f32_e32 v11, v205, v11
	v_exp_f32_e32 v219, v87
	v_fmamk_f32 v87, v102, 0x3fb8aa3b, v183
	v_add_f32_e32 v11, v211, v11
	v_exp_f32_e32 v240, v87
	v_fmamk_f32 v87, v103, 0x3fb8aa3b, v183
	v_add_f32_e32 v11, v216, v11
	v_exp_f32_e32 v241, v87
	v_fmamk_f32 v87, v104, 0x3fb8aa3b, v183
	v_add_f32_e32 v11, v217, v11
	v_exp_f32_e32 v242, v87
	v_fmamk_f32 v87, v105, 0x3fb8aa3b, v183
	v_add_f32_e32 v11, v219, v11
	v_exp_f32_e32 v243, v87
	v_fmamk_f32 v87, v122, 0x3fb8aa3b, v183
	v_add_f32_e32 v11, v240, v11
	v_exp_f32_e32 v96, v87
	v_fmamk_f32 v87, v123, 0x3fb8aa3b, v183
	v_add_f32_e32 v11, v241, v11
	v_exp_f32_e32 v97, v87
	v_fmamk_f32 v87, v124, 0x3fb8aa3b, v183
	v_add_f32_e32 v11, v242, v11
	v_exp_f32_e32 v98, v87
	v_fmamk_f32 v87, v125, 0x3fb8aa3b, v183
	v_add_f32_e32 v11, v243, v11
	v_exp_f32_e32 v99, v87
	v_fmamk_f32 v87, v118, 0x3fb8aa3b, v183
	v_add_f32_e32 v11, v96, v11
	v_exp_f32_e32 v100, v87
	v_fmamk_f32 v87, v119, 0x3fb8aa3b, v183
	v_add_f32_e32 v11, v97, v11
	v_exp_f32_e32 v101, v87
	v_fmamk_f32 v87, v120, 0x3fb8aa3b, v183
	v_add_f32_e32 v11, v98, v11
	v_exp_f32_e32 v102, v87
	v_fmamk_f32 v87, v121, 0x3fb8aa3b, v183
	v_add_f32_e32 v11, v99, v11
	v_exp_f32_e32 v103, v87
	v_add_f32_e32 v11, v100, v11
	v_add_f32_e32 v11, v101, v11
	v_add_f32_e32 v11, v102, v11
	v_add_f32_e32 v87, v103, v11
	v_fmamk_f32 v11, v106, 0x3fb8aa3b, v183
	v_exp_f32_e32 v11, v11
	v_fmamk_f32 v91, v109, 0x3fb8aa3b, v183
	v_exp_f32_e32 v91, v91
	v_fmamk_f32 v90, v90, 0x3fb8aa3b, v183
	v_add_f32_e32 v88, v11, v87
	v_fmamk_f32 v87, v107, 0x3fb8aa3b, v183
	v_exp_f32_e32 v87, v87
	v_exp_f32_e32 v92, v90
	v_fmamk_f32 v90, v127, 0x3fb8aa3b, v183
	v_exp_f32_e32 v93, v90
	v_add_f32_e32 v89, v87, v88
	v_fmamk_f32 v88, v108, 0x3fb8aa3b, v183
	v_exp_f32_e32 v88, v88
	v_fmamk_f32 v90, v149, 0x3fb8aa3b, v183
	v_exp_f32_e32 v94, v90
	v_fmac_f32_e32 v183, 0x3fb8aa3b, v182
	v_add_f32_e32 v89, v88, v89
	v_add_f32_e32 v89, v91, v89
	v_exp_f32_e32 v95, v183
	v_add_f32_e32 v89, v92, v89
	v_add_f32_e32 v89, v93, v89
	v_add_f32_e32 v89, v94, v89
	v_add_f32_e32 v89, v95, v89
	v_add_u32_e32 v124, s27, v163
	ds_bpermute_b32 v90, v175, v89
	ds_read_b64_tr_b16 v[182:183], v124
	v_add_u32_e32 v124, s26, v163
	v_cvt_pk_bf16_f32 v104, v184, v185
	ds_read_b64_tr_b16 v[184:185], v124
	v_add_u32_e32 v124, s27, v164
	v_cvt_pk_bf16_f32 v105, v186, v187
	ds_read_b64_tr_b16 v[186:187], v124
	v_add_u32_e32 v124, s26, v164
	v_cvt_pk_bf16_f32 v106, v148, v188
	v_cvt_pk_bf16_f32 v107, v189, v190
	ds_read_b64_tr_b16 v[188:189], v124
	v_add_u32_e32 v124, s27, v165
	ds_read_b64_tr_b16 v[190:191], v124
	v_add_u32_e32 v124, s26, v165
	s_waitcnt lgkmcnt(5)
	v_add_f32_e32 v89, v89, v90
	ds_read_b64_tr_b16 v[192:193], v124
	v_add_u32_e32 v124, s27, v166
	ds_bpermute_b32 v90, v176, v89
	v_add_u32_e32 v108, s27, v159
	v_add_u32_e32 v110, s26, v159
	v_add_u32_e32 v112, s27, v160
	v_add_u32_e32 v114, s26, v160
	v_add_u32_e32 v116, s27, v161
	v_add_u32_e32 v118, s26, v161
	v_add_u32_e32 v120, s27, v162
	v_add_u32_e32 v122, s26, v162
	ds_read_b64_tr_b16 v[194:195], v124
	v_add_u32_e32 v124, s26, v166
	ds_read_b64_tr_b16 v[108:109], v108
	ds_read_b64_tr_b16 v[110:111], v110
	ds_read_b64_tr_b16 v[112:113], v112
	ds_read_b64_tr_b16 v[114:115], v114
	ds_read_b64_tr_b16 v[116:117], v116
	ds_read_b64_tr_b16 v[118:119], v118
	ds_read_b64_tr_b16 v[120:121], v120
	ds_read_b64_tr_b16 v[122:123], v122
	ds_read_b64_tr_b16 v[196:197], v124
	v_mfma_f32_16x16x32_bf16 v[70:73], v[70:73], v[104:107], 0
	v_mfma_f32_16x16x32_bf16 v[2:5], v[2:5], v[104:107], 0
	v_mfma_f32_16x16x32_bf16 v[74:77], v[74:77], v[104:107], 0
	v_mfma_f32_16x16x32_bf16 v[6:9], v[6:9], v[104:107], 0
	v_mfma_f32_16x16x32_bf16 v[78:81], v[78:81], v[104:107], 0
	v_mfma_f32_16x16x32_bf16 v[12:15], v[12:15], v[104:107], 0
	v_mfma_f32_16x16x32_bf16 v[82:85], v[82:85], v[104:107], 0
	v_mfma_f32_16x16x32_bf16 v[66:69], v[66:69], v[104:107], 0
	s_add_i32 s26, s88, s61
	s_add_i32 s2, s88, s2
	v_add_u32_e32 v124, s26, v159
	v_cvt_pk_bf16_f32 v104, v198, v199
	ds_read_b64_tr_b16 v[198:199], v124
	v_add_u32_e32 v124, s2, v159
	v_cvt_pk_bf16_f32 v105, v200, v201
	ds_read_b64_tr_b16 v[200:201], v124
	v_add_u32_e32 v124, s26, v160
	v_cvt_pk_bf16_f32 v106, v202, v203
	ds_read_b64_tr_b16 v[202:203], v124
	v_add_u32_e32 v124, s2, v160
	v_cvt_pk_bf16_f32 v107, v204, v205
	ds_read_b64_tr_b16 v[204:205], v124
	v_add_u32_e32 v124, s26, v161
	ds_read_b64_tr_b16 v[212:213], v124
	v_add_u32_e32 v124, s2, v161
	ds_read_b64_tr_b16 v[214:215], v124
	v_add_u32_e32 v124, s26, v162
	ds_read_b64_tr_b16 v[220:221], v124
	v_add_u32_e32 v124, s2, v162
	ds_read_b64_tr_b16 v[222:223], v124
	v_add_u32_e32 v124, s26, v163
	ds_read_b64_tr_b16 v[224:225], v124
	v_add_u32_e32 v124, s2, v163
	ds_read_b64_tr_b16 v[226:227], v124
	v_add_u32_e32 v124, s26, v164
	ds_read_b64_tr_b16 v[228:229], v124
	v_add_u32_e32 v124, s2, v164
	ds_read_b64_tr_b16 v[230:231], v124
	v_add_u32_e32 v124, s26, v165
	ds_read_b64_tr_b16 v[232:233], v124
	v_add_u32_e32 v124, s2, v165
	ds_read_b64_tr_b16 v[234:235], v124
	v_add_u32_e32 v124, s26, v166
	ds_read_b64_tr_b16 v[236:237], v124
	v_add_u32_e32 v124, s2, v166
	ds_read_b64_tr_b16 v[238:239], v124
	s_waitcnt lgkmcnt(14)
	v_mfma_f32_16x16x32_bf16 v[70:73], v[108:111], v[104:107], v[70:73]
	v_mfma_f32_16x16x32_bf16 v[2:5], v[112:115], v[104:107], v[2:5]
	v_mfma_f32_16x16x32_bf16 v[74:77], v[116:119], v[104:107], v[74:77]
	v_mfma_f32_16x16x32_bf16 v[6:9], v[120:123], v[104:107], v[6:9]
	v_mfma_f32_16x16x32_bf16 v[78:81], v[182:185], v[104:107], v[78:81]
	v_mfma_f32_16x16x32_bf16 v[12:15], v[186:189], v[104:107], v[12:15]
	v_mfma_f32_16x16x32_bf16 v[82:85], v[190:193], v[104:107], v[82:85]
	v_mfma_f32_16x16x32_bf16 v[66:69], v[194:197], v[104:107], v[66:69]
	s_add_i32 s2, s88, s54
	s_add_i32 s26, s88, s55
	v_add_u32_e32 v124, s2, v163
	ds_read_b64_tr_b16 v[182:183], v124
	v_add_u32_e32 v124, s26, v163
	ds_read_b64_tr_b16 v[184:185], v124
	v_add_u32_e32 v124, s2, v164
	ds_read_b64_tr_b16 v[186:187], v124
	v_add_u32_e32 v124, s26, v164
	ds_read_b64_tr_b16 v[188:189], v124
	v_add_u32_e32 v124, s2, v165
	ds_read_b64_tr_b16 v[190:191], v124
	v_add_u32_e32 v124, s26, v165
	ds_read_b64_tr_b16 v[192:193], v124
	v_add_u32_e32 v124, s2, v166
	v_add_u32_e32 v108, s2, v159
	v_add_u32_e32 v110, s26, v159
	v_add_u32_e32 v112, s2, v160
	v_add_u32_e32 v114, s26, v160
	v_add_u32_e32 v116, s2, v161
	v_add_u32_e32 v118, s26, v161
	v_add_u32_e32 v120, s2, v162
	v_add_u32_e32 v122, s26, v162
	ds_read_b64_tr_b16 v[194:195], v124
	v_add_u32_e32 v124, s26, v166
	ds_read_b64_tr_b16 v[108:109], v108
	ds_read_b64_tr_b16 v[110:111], v110
	ds_read_b64_tr_b16 v[112:113], v112
	ds_read_b64_tr_b16 v[114:115], v114
	ds_read_b64_tr_b16 v[116:117], v116
	ds_read_b64_tr_b16 v[118:119], v118
	ds_read_b64_tr_b16 v[120:121], v120
	ds_read_b64_tr_b16 v[122:123], v122
	ds_read_b64_tr_b16 v[196:197], v124
	v_cvt_pk_bf16_f32 v104, v211, v216
	v_cvt_pk_bf16_f32 v105, v217, v219
	v_cvt_pk_bf16_f32 v106, v240, v241
	v_cvt_pk_bf16_f32 v107, v242, v243
	s_nop 1
	v_mfma_f32_16x16x32_bf16 v[70:73], v[198:201], v[104:107], v[70:73]
	s_waitcnt lgkmcnt(14)
	v_mfma_f32_16x16x32_bf16 v[2:5], v[202:205], v[104:107], v[2:5]
	v_mfma_f32_16x16x32_bf16 v[74:77], v[212:215], v[104:107], v[74:77]
	v_mfma_f32_16x16x32_bf16 v[6:9], v[220:223], v[104:107], v[6:9]
	v_mfma_f32_16x16x32_bf16 v[78:81], v[224:227], v[104:107], v[78:81]
	v_mfma_f32_16x16x32_bf16 v[12:15], v[228:231], v[104:107], v[12:15]
	v_mfma_f32_16x16x32_bf16 v[82:85], v[232:235], v[104:107], v[82:85]
	v_mfma_f32_16x16x32_bf16 v[66:69], v[236:239], v[104:107], v[66:69]
	s_add_i32 s2, s88, s6
	s_add_i32 s6, s88, s7
	v_add_u32_e32 v124, s2, v161
	ds_read_b64_tr_b16 v[198:199], v124
	v_add_u32_e32 v124, s6, v161
	ds_read_b64_tr_b16 v[200:201], v124
	v_add_u32_e32 v124, s2, v162
	ds_read_b64_tr_b16 v[202:203], v124
	v_add_u32_e32 v124, s6, v162
	ds_read_b64_tr_b16 v[204:205], v124
	v_add_u32_e32 v124, s2, v163
	ds_read_b64_tr_b16 v[212:213], v124
	v_add_u32_e32 v124, s6, v163
	ds_read_b64_tr_b16 v[214:215], v124
	v_add_u32_e32 v124, s2, v164
	ds_read_b64_tr_b16 v[220:221], v124
	v_add_u32_e32 v124, s6, v164
	ds_read_b64_tr_b16 v[222:223], v124
	v_add_u32_e32 v124, s2, v165
	ds_read_b64_tr_b16 v[224:225], v124
	v_add_u32_e32 v124, s6, v165
	ds_read_b64_tr_b16 v[226:227], v124
	v_add_u32_e32 v124, s2, v166
	v_cvt_pk_bf16_f32 v96, v96, v97
	v_cvt_pk_bf16_f32 v97, v98, v99
	v_cvt_pk_bf16_f32 v98, v100, v101
	v_cvt_pk_bf16_f32 v99, v102, v103
	v_add_u32_e32 v100, s2, v159
	v_add_u32_e32 v102, s6, v159
	v_add_u32_e32 v104, s2, v160
	v_add_u32_e32 v106, s6, v160
	ds_read_b64_tr_b16 v[228:229], v124
	v_add_u32_e32 v124, s6, v166
	ds_read_b64_tr_b16 v[100:101], v100
	ds_read_b64_tr_b16 v[102:103], v102
	ds_read_b64_tr_b16 v[104:105], v104
	ds_read_b64_tr_b16 v[106:107], v106
	ds_read_b64_tr_b16 v[230:231], v124
	s_waitcnt lgkmcnt(14)
	v_mfma_f32_16x16x32_bf16 v[70:73], v[108:111], v[96:99], v[70:73]
	v_mfma_f32_16x16x32_bf16 v[2:5], v[112:115], v[96:99], v[2:5]
	v_mfma_f32_16x16x32_bf16 v[74:77], v[116:119], v[96:99], v[74:77]
	v_mfma_f32_16x16x32_bf16 v[6:9], v[120:123], v[96:99], v[6:9]
	v_mfma_f32_16x16x32_bf16 v[12:15], v[186:189], v[96:99], v[12:15]
	v_mfma_f32_16x16x32_bf16 v[108:111], v[182:185], v[96:99], v[78:81]
	v_mfma_f32_16x16x32_bf16 v[112:115], v[190:193], v[96:99], v[82:85]
	v_mfma_f32_16x16x32_bf16 v[96:99], v[194:197], v[96:99], v[66:69]
	v_cvt_pk_bf16_f32 v116, v11, v87
	v_cvt_pk_bf16_f32 v117, v88, v91
	v_cvt_pk_bf16_f32 v118, v92, v93
	v_cvt_pk_bf16_f32 v119, v94, v95
	s_waitcnt lgkmcnt(3)
	s_nop 0
	v_mfma_f32_16x16x32_bf16 v[82:85], v[100:103], v[116:119], v[70:73]
	s_waitcnt lgkmcnt(1)
	v_mfma_f32_16x16x32_bf16 v[78:81], v[104:107], v[116:119], v[2:5]
	v_mfma_f32_16x16x32_bf16 v[74:77], v[198:201], v[116:119], v[74:77]
	v_mfma_f32_16x16x32_bf16 v[70:73], v[202:205], v[116:119], v[6:9]
	v_mfma_f32_16x16x32_bf16 v[66:69], v[212:215], v[116:119], v[108:111]
	v_mfma_f32_16x16x32_bf16 v[12:15], v[220:223], v[116:119], v[12:15]
	v_mfma_f32_16x16x32_bf16 v[6:9], v[224:227], v[116:119], v[112:115]
	s_waitcnt lgkmcnt(0)
	v_mfma_f32_16x16x32_bf16 v[2:5], v[228:231], v[116:119], v[96:99]
	s_and_saveexec_b64 s[6:7], s[0:1]
	s_cbranch_execz .LBB0_1074
	v_lshl_add_u64 v[92:93], s[52:53], 0, v[16:17]
	v_lshl_add_u64 v[92:93], v[92:93], 3, s[8:9]
	v_add_f32_e32 v87, v89, v90
	global_store_dwordx2 v[92:93], v[86:87], off

.LBB0_1098:
	s_cmp_eq_u32 s60, 0
	s_cselect_b64 vcc, -1, 0
	v_cndmask_b32_e32 v11, 0, v169, vcc
	v_sub_u32_e32 v16, 0x80, v11
	v_add_u32_e32 v11, v168, v11
	v_sub_u32_e32 v11, v150, v11
	v_add_u32_e32 v17, s68, v11
	v_cmp_le_u32_e32 vcc, v17, v16
	v_add_u32_e32 v127, 1, v17
	v_add_u32_e32 v182, 2, v17
	v_cndmask_b32_e32 v98, v181, v98, vcc
	v_cmp_le_u32_e32 vcc, v127, v16
	v_add_u32_e32 v17, 3, v17
	s_add_i32 s26, s88, s26
	v_cndmask_b32_e32 v99, v181, v99, vcc
	v_cmp_le_u32_e32 vcc, v182, v16
	v_max3_f32 v127, v98, s90, v99
	s_add_i32 s27, s88, s27
	v_cndmask_b32_e32 v100, v181, v100, vcc
	v_cmp_le_u32_e32 vcc, v17, v16
	s_nop 1
	v_cndmask_b32_e32 v101, v181, v101, vcc
	v_max3_f32 v17, v127, v100, v101
	v_add_u32_e32 v127, s69, v11
	v_cmp_le_u32_e32 vcc, v127, v16
	s_nop 1
	v_cndmask_b32_e32 v182, v181, v86, vcc
	v_add_u32_e32 v86, 1, v127
	v_cmp_le_u32_e32 vcc, v86, v16
	v_add_u32_e32 v86, 2, v127
	s_nop 0
	v_cndmask_b32_e32 v87, v181, v87, vcc
	v_cmp_le_u32_e32 vcc, v86, v16
	v_add_u32_e32 v86, 3, v127
	v_max3_f32 v17, v17, v182, v87
	v_cndmask_b32_e32 v88, v181, v88, vcc
	v_cmp_le_u32_e32 vcc, v86, v16
	v_add_u32_e32 v86, s72, v11
	v_add_u32_e32 v127, 1, v86
	v_cndmask_b32_e32 v89, v181, v89, vcc
	v_cmp_le_u32_e32 vcc, v86, v16
	v_max3_f32 v17, v17, v88, v89
	s_nop 0
	v_cndmask_b32_e32 v110, v181, v110, vcc
	v_cmp_le_u32_e32 vcc, v127, v16
	v_add_u32_e32 v127, 2, v86
	v_add_u32_e32 v86, 3, v86
	v_cndmask_b32_e32 v111, v181, v111, vcc
	v_cmp_le_u32_e32 vcc, v127, v16
	v_max3_f32 v17, v17, v110, v111
	s_nop 0
	v_cndmask_b32_e32 v112, v181, v112, vcc
	v_cmp_le_u32_e32 vcc, v86, v16
	v_add_u32_e32 v86, s73, v11
	v_add_u32_e32 v127, 1, v86
	v_cndmask_b32_e32 v113, v181, v113, vcc
	v_cmp_le_u32_e32 vcc, v86, v16
	v_max3_f32 v17, v17, v112, v113
	s_nop 0
	v_cndmask_b32_e32 v94, v181, v94, vcc
	v_cmp_le_u32_e32 vcc, v127, v16
	v_add_u32_e32 v127, 2, v86
	v_add_u32_e32 v86, 3, v86
	v_cndmask_b32_e32 v95, v181, v95, vcc
	v_cmp_le_u32_e32 vcc, v127, v16
	v_max3_f32 v17, v17, v94, v95
	s_nop 0
	v_cndmask_b32_e32 v96, v181, v96, vcc
	v_cmp_le_u32_e32 vcc, v86, v16
	v_add_u32_e32 v86, s80, v11
	v_add_u32_e32 v127, 1, v86
	v_cndmask_b32_e32 v97, v181, v97, vcc
	v_cmp_le_u32_e32 vcc, v86, v16
	v_max3_f32 v17, v17, v96, v97
	s_nop 0
	v_cndmask_b32_e32 v114, v181, v114, vcc
	v_cmp_le_u32_e32 vcc, v127, v16
	v_add_u32_e32 v127, 2, v86
	v_add_u32_e32 v86, 3, v86
	v_cndmask_b32_e32 v115, v181, v115, vcc
	v_cmp_le_u32_e32 vcc, v127, v16
	v_max3_f32 v17, v17, v114, v115
	s_nop 0
	v_cndmask_b32_e32 v116, v181, v116, vcc
	v_cmp_le_u32_e32 vcc, v86, v16
	v_add_u32_e32 v86, s81, v11
	v_add_u32_e32 v127, 1, v86
	v_cndmask_b32_e32 v117, v181, v117, vcc
	v_cmp_le_u32_e32 vcc, v86, v16
	v_max3_f32 v17, v17, v116, v117
	s_nop 0
	v_cndmask_b32_e32 v102, v181, v102, vcc
	v_cmp_le_u32_e32 vcc, v127, v16
	v_add_u32_e32 v127, 2, v86
	v_add_u32_e32 v86, 3, v86
	v_cndmask_b32_e32 v103, v181, v103, vcc
	v_cmp_le_u32_e32 vcc, v127, v16
	v_max3_f32 v17, v17, v102, v103
	s_nop 0
	v_cndmask_b32_e32 v104, v181, v104, vcc
	v_cmp_le_u32_e32 vcc, v86, v16
	v_add_u32_e32 v86, s84, v11
	v_add_u32_e32 v127, 1, v86
	v_cndmask_b32_e32 v105, v181, v105, vcc
	v_cmp_le_u32_e32 vcc, v86, v16
	v_max3_f32 v17, v17, v104, v105
	s_nop 0
	v_cndmask_b32_e32 v122, v181, v122, vcc
	v_cmp_le_u32_e32 vcc, v127, v16
	v_add_u32_e32 v127, 2, v86
	v_add_u32_e32 v86, 3, v86
	v_cndmask_b32_e32 v123, v181, v123, vcc
	v_cmp_le_u32_e32 vcc, v127, v16
	v_max3_f32 v17, v17, v122, v123
	s_nop 0
	v_cndmask_b32_e32 v124, v181, v124, vcc
	v_cmp_le_u32_e32 vcc, v86, v16
	v_add_u32_e32 v86, s85, v11
	v_add_u32_e32 v127, 1, v86
	v_cndmask_b32_e32 v125, v181, v125, vcc
	v_cmp_le_u32_e32 vcc, v86, v16
	v_max3_f32 v17, v17, v124, v125
	s_nop 0
	v_cndmask_b32_e32 v118, v181, v118, vcc
	v_cmp_le_u32_e32 vcc, v127, v16
	v_add_u32_e32 v127, 2, v86
	v_add_u32_e32 v86, 3, v86
	v_cndmask_b32_e32 v119, v181, v119, vcc
	v_cmp_le_u32_e32 vcc, v127, v16
	v_max3_f32 v17, v17, v118, v119
	s_nop 0
	v_cndmask_b32_e32 v120, v181, v120, vcc
	v_cmp_le_u32_e32 vcc, v86, v16
	v_add_u32_e32 v86, s86, v11
	v_add_u32_e32 v127, 1, v86
	v_cndmask_b32_e32 v121, v181, v121, vcc
	v_cmp_le_u32_e32 vcc, v86, v16
	v_add_u32_e32 v11, s87, v11
	v_max3_f32 v17, v17, v120, v121
	v_cndmask_b32_e32 v106, v181, v106, vcc
	v_cmp_le_u32_e32 vcc, v127, v16
	v_add_u32_e32 v127, 2, v86
	v_add_u32_e32 v86, 3, v86
	v_cndmask_b32_e32 v107, v181, v107, vcc
	v_cmp_le_u32_e32 vcc, v127, v16
	v_max3_f32 v17, v17, v106, v107
	s_nop 0
	v_cndmask_b32_e32 v108, v181, v108, vcc
	v_cmp_le_u32_e32 vcc, v86, v16
	v_add_u32_e32 v86, 1, v11
	s_nop 0
	v_cndmask_b32_e32 v109, v181, v109, vcc
	v_cmp_le_u32_e32 vcc, v11, v16
	v_max3_f32 v17, v17, v108, v109
	s_nop 0
	v_cndmask_b32_e32 v90, v181, v90, vcc
	v_cmp_le_u32_e32 vcc, v86, v16
	v_add_u32_e32 v86, 2, v11
	v_add_u32_e32 v11, 3, v11
	v_cndmask_b32_e32 v127, v181, v91, vcc
	v_cmp_le_u32_e32 vcc, v86, v16
	s_nop 1
	v_cndmask_b32_e32 v183, v181, v92, vcc
	v_cmp_le_u32_e32 vcc, v11, v16
	v_max3_f32 v11, v17, v90, v127
	v_add_u32_e32 v16, s12, v168
	v_cndmask_b32_e32 v184, v181, v93, vcc
	v_max3_f32 v11, v11, v183, v184
	v_mov_b32_e32 v86, v11
	v_add_u32_e32 v16, 0xffffff80, v16
	v_ashrrev_i32_e32 v17, 31, v16
	s_nop 1
	v_permlane16_swap_b32_e32 v86, v11
	v_max_f32_e32 v11, v11, v86
	v_mov_b32_e32 v86, v11
	s_nop 1
	v_permlane32_swap_b32_e32 v86, v11
	s_waitcnt lgkmcnt(0)
	v_max_f32_e32 v86, v11, v86
	v_mul_f32_e32 v185, 0xbfb8aa3b, v86
	v_fmamk_f32 v11, v98, 0x3fb8aa3b, v185
	v_exp_f32_e32 v186, v11
	v_fmamk_f32 v91, v99, 0x3fb8aa3b, v185
	v_exp_f32_e32 v187, v91
	v_fmamk_f32 v91, v100, 0x3fb8aa3b, v185
	v_exp_f32_e32 v188, v91
	v_fmamk_f32 v91, v101, 0x3fb8aa3b, v185
	v_exp_f32_e32 v189, v91
	v_fmamk_f32 v91, v182, 0x3fb8aa3b, v185
	v_add_f32_e32 v11, 0, v186
	v_exp_f32_e32 v182, v91
	v_fmamk_f32 v87, v87, 0x3fb8aa3b, v185
	v_add_f32_e32 v11, v187, v11
	v_exp_f32_e32 v190, v87
	v_fmamk_f32 v87, v88, 0x3fb8aa3b, v185
	v_add_f32_e32 v11, v188, v11
	v_exp_f32_e32 v191, v87
	v_fmamk_f32 v87, v89, 0x3fb8aa3b, v185
	v_add_f32_e32 v11, v189, v11
	v_exp_f32_e32 v192, v87
	v_fmamk_f32 v87, v110, 0x3fb8aa3b, v185
	v_add_f32_e32 v11, v182, v11
	v_exp_f32_e32 v198, v87
	v_fmamk_f32 v87, v111, 0x3fb8aa3b, v185
	v_add_f32_e32 v11, v190, v11
	v_exp_f32_e32 v199, v87
	v_fmamk_f32 v87, v112, 0x3fb8aa3b, v185
	v_add_f32_e32 v11, v191, v11
	v_exp_f32_e32 v200, v87
	v_fmamk_f32 v87, v113, 0x3fb8aa3b, v185
	v_add_f32_e32 v11, v192, v11
	v_exp_f32_e32 v201, v87
	v_fmamk_f32 v87, v94, 0x3fb8aa3b, v185
	v_add_f32_e32 v11, v198, v11
	v_exp_f32_e32 v202, v87
	v_fmamk_f32 v87, v95, 0x3fb8aa3b, v185
	v_add_f32_e32 v11, v199, v11
	v_exp_f32_e32 v203, v87
	v_fmamk_f32 v87, v96, 0x3fb8aa3b, v185
	v_add_f32_e32 v11, v200, v11
	v_exp_f32_e32 v204, v87
	v_fmamk_f32 v87, v97, 0x3fb8aa3b, v185
	v_add_f32_e32 v11, v201, v11
	v_exp_f32_e32 v205, v87
	v_fmamk_f32 v87, v114, 0x3fb8aa3b, v185
	v_add_f32_e32 v11, v202, v11
	v_exp_f32_e32 v211, v87
	v_fmamk_f32 v87, v115, 0x3fb8aa3b, v185
	v_add_f32_e32 v11, v203, v11
	v_exp_f32_e32 v216, v87
	v_fmamk_f32 v87, v116, 0x3fb8aa3b, v185
	v_add_f32_e32 v11, v204, v11
	v_exp_f32_e32 v217, v87
	v_fmamk_f32 v87, v117, 0x3fb8aa3b, v185
	v_add_f32_e32 v11, v205, v11
	v_exp_f32_e32 v219, v87
	v_fmamk_f32 v87, v102, 0x3fb8aa3b, v185
	v_add_f32_e32 v11, v211, v11
	v_exp_f32_e32 v240, v87
	v_fmamk_f32 v87, v103, 0x3fb8aa3b, v185
	v_add_f32_e32 v11, v216, v11
	v_exp_f32_e32 v241, v87
	v_fmamk_f32 v87, v104, 0x3fb8aa3b, v185
	v_add_f32_e32 v11, v217, v11
	v_exp_f32_e32 v242, v87
	v_fmamk_f32 v87, v105, 0x3fb8aa3b, v185
	v_add_f32_e32 v11, v219, v11
	v_exp_f32_e32 v243, v87
	v_fmamk_f32 v87, v122, 0x3fb8aa3b, v185
	v_add_f32_e32 v11, v240, v11
	v_exp_f32_e32 v96, v87
	v_fmamk_f32 v87, v123, 0x3fb8aa3b, v185
	v_add_f32_e32 v11, v241, v11
	v_exp_f32_e32 v97, v87
	v_fmamk_f32 v87, v124, 0x3fb8aa3b, v185
	v_add_f32_e32 v11, v242, v11
	v_exp_f32_e32 v98, v87
	v_fmamk_f32 v87, v125, 0x3fb8aa3b, v185
	v_add_f32_e32 v11, v243, v11
	v_exp_f32_e32 v99, v87
	v_fmamk_f32 v87, v118, 0x3fb8aa3b, v185
	v_add_f32_e32 v11, v96, v11
	v_exp_f32_e32 v100, v87
	v_fmamk_f32 v87, v119, 0x3fb8aa3b, v185
	v_add_f32_e32 v11, v97, v11
	v_exp_f32_e32 v101, v87
	v_fmamk_f32 v87, v120, 0x3fb8aa3b, v185
	v_add_f32_e32 v11, v98, v11
	v_exp_f32_e32 v102, v87
	v_fmamk_f32 v87, v121, 0x3fb8aa3b, v185
	v_add_f32_e32 v11, v99, v11
	v_exp_f32_e32 v103, v87
	v_add_f32_e32 v11, v100, v11
	v_add_f32_e32 v11, v101, v11
	v_add_f32_e32 v11, v102, v11
	v_add_f32_e32 v87, v103, v11
	v_fmamk_f32 v11, v106, 0x3fb8aa3b, v185
	v_exp_f32_e32 v11, v11
	v_fmamk_f32 v91, v109, 0x3fb8aa3b, v185
	v_exp_f32_e32 v91, v91
	v_fmamk_f32 v90, v90, 0x3fb8aa3b, v185
	v_add_f32_e32 v88, v11, v87
	v_fmamk_f32 v87, v107, 0x3fb8aa3b, v185
	v_exp_f32_e32 v87, v87
	v_exp_f32_e32 v92, v90
	v_fmamk_f32 v90, v127, 0x3fb8aa3b, v185
	v_exp_f32_e32 v93, v90
	v_add_f32_e32 v89, v87, v88
	v_fmamk_f32 v88, v108, 0x3fb8aa3b, v185
	v_exp_f32_e32 v88, v88
	v_fmamk_f32 v90, v183, 0x3fb8aa3b, v185
	v_exp_f32_e32 v94, v90
	v_fmac_f32_e32 v185, 0x3fb8aa3b, v184
	v_add_f32_e32 v89, v88, v89
	v_add_f32_e32 v89, v91, v89
	v_exp_f32_e32 v95, v185
	v_add_f32_e32 v89, v92, v89
	v_add_f32_e32 v89, v93, v89
	v_add_f32_e32 v89, v94, v89
	v_add_f32_e32 v89, v95, v89
	v_add_u32_e32 v124, s26, v163
	ds_bpermute_b32 v90, v175, v89
	v_cvt_pk_bf16_f32 v106, v182, v190
	ds_read_b64_tr_b16 v[182:183], v124
	v_add_u32_e32 v124, s27, v163
	ds_read_b64_tr_b16 v[184:185], v124
	v_add_u32_e32 v124, s26, v164
	v_cvt_pk_bf16_f32 v104, v186, v187
	ds_read_b64_tr_b16 v[186:187], v124
	v_add_u32_e32 v124, s27, v164
	v_cvt_pk_bf16_f32 v105, v188, v189
	ds_read_b64_tr_b16 v[188:189], v124
	v_add_u32_e32 v124, s26, v165
	v_cvt_pk_bf16_f32 v107, v191, v192
	ds_read_b64_tr_b16 v[190:191], v124
	v_add_u32_e32 v124, s27, v165
	s_waitcnt lgkmcnt(5)
	v_add_f32_e32 v89, v89, v90
	ds_read_b64_tr_b16 v[192:193], v124
	v_add_u32_e32 v124, s26, v166
	ds_bpermute_b32 v90, v176, v89
	v_add_u32_e32 v108, s26, v159
	v_add_u32_e32 v110, s27, v159
	v_add_u32_e32 v112, s26, v160
	v_add_u32_e32 v114, s27, v160
	v_add_u32_e32 v116, s26, v161
	v_add_u32_e32 v118, s27, v161
	v_add_u32_e32 v120, s26, v162
	v_add_u32_e32 v122, s27, v162
	ds_read_b64_tr_b16 v[194:195], v124
	v_add_u32_e32 v124, s27, v166
	ds_read_b64_tr_b16 v[108:109], v108
	ds_read_b64_tr_b16 v[110:111], v110
	ds_read_b64_tr_b16 v[112:113], v112
	ds_read_b64_tr_b16 v[114:115], v114
	ds_read_b64_tr_b16 v[116:117], v116
	ds_read_b64_tr_b16 v[118:119], v118
	ds_read_b64_tr_b16 v[120:121], v120
	ds_read_b64_tr_b16 v[122:123], v122
	ds_read_b64_tr_b16 v[196:197], v124
	v_mfma_f32_16x16x32_bf16 v[70:73], v[70:73], v[104:107], 0
	v_mfma_f32_16x16x32_bf16 v[2:5], v[2:5], v[104:107], 0
	v_mfma_f32_16x16x32_bf16 v[74:77], v[74:77], v[104:107], 0
	v_mfma_f32_16x16x32_bf16 v[6:9], v[6:9], v[104:107], 0
	v_mfma_f32_16x16x32_bf16 v[78:81], v[78:81], v[104:107], 0
	v_mfma_f32_16x16x32_bf16 v[12:15], v[12:15], v[104:107], 0
	v_mfma_f32_16x16x32_bf16 v[82:85], v[82:85], v[104:107], 0
	v_mfma_f32_16x16x32_bf16 v[66:69], v[66:69], v[104:107], 0
	s_add_i32 s2, s88, s2
	s_add_i32 s26, s88, s56
	v_add_u32_e32 v124, s2, v159
	v_cvt_pk_bf16_f32 v104, v198, v199
	ds_read_b64_tr_b16 v[198:199], v124
	v_add_u32_e32 v124, s26, v159
	v_cvt_pk_bf16_f32 v105, v200, v201
	ds_read_b64_tr_b16 v[200:201], v124
	v_add_u32_e32 v124, s2, v160
	v_cvt_pk_bf16_f32 v106, v202, v203
	ds_read_b64_tr_b16 v[202:203], v124
	v_add_u32_e32 v124, s26, v160
	v_cvt_pk_bf16_f32 v107, v204, v205
	ds_read_b64_tr_b16 v[204:205], v124
	v_add_u32_e32 v124, s2, v161
	ds_read_b64_tr_b16 v[212:213], v124
	v_add_u32_e32 v124, s26, v161
	ds_read_b64_tr_b16 v[214:215], v124
	v_add_u32_e32 v124, s2, v162
	ds_read_b64_tr_b16 v[220:221], v124
	v_add_u32_e32 v124, s26, v162
	ds_read_b64_tr_b16 v[222:223], v124
	v_add_u32_e32 v124, s2, v163
	ds_read_b64_tr_b16 v[224:225], v124
	v_add_u32_e32 v124, s26, v163
	ds_read_b64_tr_b16 v[226:227], v124
	v_add_u32_e32 v124, s2, v164
	ds_read_b64_tr_b16 v[228:229], v124
	v_add_u32_e32 v124, s26, v164
	ds_read_b64_tr_b16 v[230:231], v124
	v_add_u32_e32 v124, s2, v165
	ds_read_b64_tr_b16 v[232:233], v124
	v_add_u32_e32 v124, s26, v165
	ds_read_b64_tr_b16 v[234:235], v124
	v_add_u32_e32 v124, s2, v166
	ds_read_b64_tr_b16 v[236:237], v124
	v_add_u32_e32 v124, s26, v166
	ds_read_b64_tr_b16 v[238:239], v124
	s_waitcnt lgkmcnt(14)
	v_mfma_f32_16x16x32_bf16 v[70:73], v[108:111], v[104:107], v[70:73]
	v_mfma_f32_16x16x32_bf16 v[2:5], v[112:115], v[104:107], v[2:5]
	v_mfma_f32_16x16x32_bf16 v[74:77], v[116:119], v[104:107], v[74:77]
	v_mfma_f32_16x16x32_bf16 v[6:9], v[120:123], v[104:107], v[6:9]
	v_mfma_f32_16x16x32_bf16 v[78:81], v[182:185], v[104:107], v[78:81]
	v_mfma_f32_16x16x32_bf16 v[12:15], v[186:189], v[104:107], v[12:15]
	v_mfma_f32_16x16x32_bf16 v[82:85], v[190:193], v[104:107], v[82:85]
	v_mfma_f32_16x16x32_bf16 v[66:69], v[194:197], v[104:107], v[66:69]
	s_add_i32 s2, s88, s10
	s_add_i32 s10, s88, s33
	v_add_u32_e32 v124, s2, v163
	ds_read_b64_tr_b16 v[182:183], v124
	v_add_u32_e32 v124, s10, v163
	ds_read_b64_tr_b16 v[184:185], v124
	v_add_u32_e32 v124, s2, v164
	ds_read_b64_tr_b16 v[186:187], v124
	v_add_u32_e32 v124, s10, v164
	ds_read_b64_tr_b16 v[188:189], v124
	v_add_u32_e32 v124, s2, v165
	ds_read_b64_tr_b16 v[190:191], v124
	v_add_u32_e32 v124, s10, v165
	ds_read_b64_tr_b16 v[192:193], v124
	v_add_u32_e32 v124, s2, v166
	v_add_u32_e32 v108, s2, v159
	v_add_u32_e32 v110, s10, v159
	v_add_u32_e32 v112, s2, v160
	v_add_u32_e32 v114, s10, v160
	v_add_u32_e32 v116, s2, v161
	v_add_u32_e32 v118, s10, v161
	v_add_u32_e32 v120, s2, v162
	v_add_u32_e32 v122, s10, v162
	ds_read_b64_tr_b16 v[194:195], v124
	v_add_u32_e32 v124, s10, v166
	ds_read_b64_tr_b16 v[108:109], v108
	ds_read_b64_tr_b16 v[110:111], v110
	ds_read_b64_tr_b16 v[112:113], v112
	ds_read_b64_tr_b16 v[114:115], v114
	ds_read_b64_tr_b16 v[116:117], v116
	ds_read_b64_tr_b16 v[118:119], v118
	ds_read_b64_tr_b16 v[120:121], v120
	ds_read_b64_tr_b16 v[122:123], v122
	ds_read_b64_tr_b16 v[196:197], v124
	v_cvt_pk_bf16_f32 v104, v211, v216
	v_cvt_pk_bf16_f32 v105, v217, v219
	v_cvt_pk_bf16_f32 v106, v240, v241
	v_cvt_pk_bf16_f32 v107, v242, v243
	s_nop 1
	v_mfma_f32_16x16x32_bf16 v[70:73], v[198:201], v[104:107], v[70:73]
	s_waitcnt lgkmcnt(14)
	v_mfma_f32_16x16x32_bf16 v[2:5], v[202:205], v[104:107], v[2:5]
	v_mfma_f32_16x16x32_bf16 v[74:77], v[212:215], v[104:107], v[74:77]
	v_mfma_f32_16x16x32_bf16 v[6:9], v[220:223], v[104:107], v[6:9]
	v_mfma_f32_16x16x32_bf16 v[78:81], v[224:227], v[104:107], v[78:81]
	v_mfma_f32_16x16x32_bf16 v[12:15], v[228:231], v[104:107], v[12:15]
	v_mfma_f32_16x16x32_bf16 v[82:85], v[232:235], v[104:107], v[82:85]
	v_mfma_f32_16x16x32_bf16 v[66:69], v[236:239], v[104:107], v[66:69]
	s_add_i32 s2, s88, s6
	s_add_i32 s6, s88, s7
	v_add_u32_e32 v124, s2, v161
	ds_read_b64_tr_b16 v[198:199], v124
	v_add_u32_e32 v124, s6, v161
	ds_read_b64_tr_b16 v[200:201], v124
	v_add_u32_e32 v124, s2, v162
	ds_read_b64_tr_b16 v[202:203], v124
	v_add_u32_e32 v124, s6, v162
	ds_read_b64_tr_b16 v[204:205], v124
	v_add_u32_e32 v124, s2, v163
	ds_read_b64_tr_b16 v[212:213], v124
	v_add_u32_e32 v124, s6, v163
	ds_read_b64_tr_b16 v[214:215], v124
	v_add_u32_e32 v124, s2, v164
	ds_read_b64_tr_b16 v[220:221], v124
	v_add_u32_e32 v124, s6, v164
	ds_read_b64_tr_b16 v[222:223], v124
	v_add_u32_e32 v124, s2, v165
	ds_read_b64_tr_b16 v[224:225], v124
	v_add_u32_e32 v124, s6, v165
	ds_read_b64_tr_b16 v[226:227], v124
	v_add_u32_e32 v124, s2, v166
	v_cvt_pk_bf16_f32 v96, v96, v97
	v_cvt_pk_bf16_f32 v97, v98, v99
	v_cvt_pk_bf16_f32 v98, v100, v101
	v_cvt_pk_bf16_f32 v99, v102, v103
	v_add_u32_e32 v100, s2, v159
	v_add_u32_e32 v102, s6, v159
	v_add_u32_e32 v104, s2, v160
	v_add_u32_e32 v106, s6, v160
	ds_read_b64_tr_b16 v[228:229], v124
	v_add_u32_e32 v124, s6, v166
	ds_read_b64_tr_b16 v[100:101], v100
	ds_read_b64_tr_b16 v[102:103], v102
	ds_read_b64_tr_b16 v[104:105], v104
	ds_read_b64_tr_b16 v[106:107], v106
	ds_read_b64_tr_b16 v[230:231], v124
	s_waitcnt lgkmcnt(14)
	v_mfma_f32_16x16x32_bf16 v[70:73], v[108:111], v[96:99], v[70:73]
	v_mfma_f32_16x16x32_bf16 v[2:5], v[112:115], v[96:99], v[2:5]
	v_mfma_f32_16x16x32_bf16 v[74:77], v[116:119], v[96:99], v[74:77]
	v_mfma_f32_16x16x32_bf16 v[6:9], v[120:123], v[96:99], v[6:9]
	v_mfma_f32_16x16x32_bf16 v[12:15], v[186:189], v[96:99], v[12:15]
	v_mfma_f32_16x16x32_bf16 v[108:111], v[182:185], v[96:99], v[78:81]
	v_mfma_f32_16x16x32_bf16 v[112:115], v[190:193], v[96:99], v[82:85]
	v_mfma_f32_16x16x32_bf16 v[96:99], v[194:197], v[96:99], v[66:69]
	v_cvt_pk_bf16_f32 v116, v11, v87
	v_cvt_pk_bf16_f32 v117, v88, v91
	v_cvt_pk_bf16_f32 v118, v92, v93
	v_cvt_pk_bf16_f32 v119, v94, v95
	s_waitcnt lgkmcnt(3)
	s_nop 0
	v_mfma_f32_16x16x32_bf16 v[82:85], v[100:103], v[116:119], v[70:73]
	s_waitcnt lgkmcnt(1)
	v_mfma_f32_16x16x32_bf16 v[78:81], v[104:107], v[116:119], v[2:5]
	v_mfma_f32_16x16x32_bf16 v[74:77], v[198:201], v[116:119], v[74:77]
	v_mfma_f32_16x16x32_bf16 v[70:73], v[202:205], v[116:119], v[6:9]
	v_mfma_f32_16x16x32_bf16 v[66:69], v[212:215], v[116:119], v[108:111]
	v_mfma_f32_16x16x32_bf16 v[12:15], v[220:223], v[116:119], v[12:15]
	v_mfma_f32_16x16x32_bf16 v[6:9], v[224:227], v[116:119], v[112:115]
	s_waitcnt lgkmcnt(0)
	v_mfma_f32_16x16x32_bf16 v[2:5], v[228:231], v[116:119], v[96:99]
	s_and_saveexec_b64 s[6:7], s[0:1]
	s_cbranch_execz .LBB0_1100
	v_lshl_add_u64 v[92:93], s[52:53], 0, v[16:17]
	v_lshl_add_u64 v[92:93], v[92:93], 3, s[8:9]
	v_add_f32_e32 v87, v89, v90
	global_store_dwordx2 v[92:93], v[86:87], off
